# additionally defer tile-1 y rows 64-95 (8 MB) from scan 2 to scan 3 producer waves
# baseline (speedup 1.0000x reference)
.LBB1_107:
	s_and_b32 s4, vcc_lo, 0x7fff8000
	s_and_b32 s10, s99, 0x60
	s_or_b32 s4, s10, s4
	s_mov_b64 s[92:93], s[18:19]
	s_mov_b64 s[90:91], s[14:15]
	s_add_i32 s4, s4, s98
	s_mov_b32 s27, s5
	v_mov_b32_e32 v165, s3
	s_or_b32 s26, s4, 14
	s_mov_b32 s97, s5
	s_mov_b32 s95, s5
	s_mov_b32 s89, s5
	s_mov_b32 s79, s5
	s_mov_b32 s77, s5
	s_mov_b32 s71, s5
	s_mov_b32 s63, s5
	s_mov_b32 s61, s5
	s_mov_b32 s57, s5
	s_mov_b32 s45, s5
	s_mov_b32 s43, s5
	s_mov_b32 s39, s5
	s_mov_b32 s31, s5
	v_lshl_add_u64 v[140:141], s[90:91], 0, v[162:163]
	v_lshl_add_u64 v[130:131], s[92:93], 0, v[162:163]
	s_lshl_b64 s[92:93], s[4:5], 10
	s_or_b32 s96, s4, 1
	s_or_b32 s94, s4, 2
	s_or_b32 s88, s4, 3
	s_or_b32 s78, s4, 4
	s_or_b32 s76, s4, 5
	s_or_b32 s70, s4, 6
	s_or_b32 s62, s4, 7
	s_or_b32 s60, s4, 8
	s_or_b32 s56, s4, 9
	s_or_b32 s44, s4, 10
	s_or_b32 s42, s4, 11
	s_or_b32 s38, s4, 12
	s_or_b32 s30, s4, 13
	ds_read_b128 v[132:135], v165
	ds_read_b128 v[136:139], v165 offset:16
	s_or_b32 s4, s4, 15
	s_lshl_b64 s[26:27], s[26:27], 10
	s_lshl_b64 s[96:97], s[96:97], 10
	s_lshl_b64 s[94:95], s[94:95], 10
	s_lshl_b64 s[88:89], s[88:89], 10
	s_lshl_b64 s[78:79], s[78:79], 10
	s_lshl_b64 s[76:77], s[76:77], 10
	s_lshl_b64 s[70:71], s[70:71], 10
	s_lshl_b64 s[62:63], s[62:63], 10
	s_lshl_b64 s[60:61], s[60:61], 10
	s_lshl_b64 s[56:57], s[56:57], 10
	s_lshl_b64 s[44:45], s[44:45], 10
	s_lshl_b64 s[42:43], s[42:43], 10
	s_lshl_b64 s[38:39], s[38:39], 10
	s_lshl_b64 s[30:31], s[30:31], 10
	v_lshl_add_u64 v[180:181], v[140:141], 0, s[26:27]
	s_lshl_b64 s[26:27], s[4:5], 10
	v_lshl_add_u64 v[148:149], v[140:141], 0, s[92:93]
	v_lshl_add_u64 v[150:151], v[140:141], 0, s[96:97]
	v_lshl_add_u64 v[152:153], v[140:141], 0, s[94:95]
	v_lshl_add_u64 v[154:155], v[140:141], 0, s[88:89]
	v_lshl_add_u64 v[156:157], v[140:141], 0, s[78:79]
	v_lshl_add_u64 v[158:159], v[140:141], 0, s[76:77]
	v_lshl_add_u64 v[160:161], v[140:141], 0, s[70:71]
	v_lshl_add_u64 v[166:167], v[140:141], 0, s[62:63]
	v_lshl_add_u64 v[168:169], v[140:141], 0, s[60:61]
	v_lshl_add_u64 v[170:171], v[140:141], 0, s[56:57]
	v_lshl_add_u64 v[172:173], v[140:141], 0, s[44:45]
	v_lshl_add_u64 v[174:175], v[140:141], 0, s[42:43]
	v_lshl_add_u64 v[176:177], v[140:141], 0, s[38:39]
	v_lshl_add_u64 v[178:179], v[140:141], 0, s[30:31]
	v_lshl_add_u64 v[182:183], v[140:141], 0, s[26:27]
	ds_read_b128 v[140:143], v165 offset:32
	ds_read_b128 v[144:147], v165 offset:48
	s_add_i32 s22, vcc_lo, 0x1000
	s_add_i32 s24, s99, 16
	s_waitcnt lgkmcnt(3)
	v_readfirstlane_b32 s4, v132
	s_lshl_b64 s[26:27], s[4:5], 10
	s_and_b32 s4, s22, 0x7fff8000
	s_and_b32 s10, s24, 0x70
	s_mov_b32 s11, s5
	v_lshl_add_u64 v[184:185], v[130:131], 0, s[26:27]
	s_or_b32 s26, s10, s4
	v_readfirstlane_b32 s10, v133
	s_mov_b32 s23, s5
	s_mov_b32 s25, s5
	s_mov_b32 s29, s5
	s_mov_b32 s35, s5
	s_mov_b32 s37, s5
	s_mov_b32 s47, s5
	s_mov_b32 s51, s5
	s_mov_b32 s55, s5
	s_mov_b32 s69, s5
	s_mov_b32 s73, s5
	s_mov_b32 s81, s5
	v_readfirstlane_b32 s22, v134
	v_readfirstlane_b32 s24, v135
	s_waitcnt lgkmcnt(2)
	v_readfirstlane_b32 s28, v137
	v_readfirstlane_b32 s34, v138
	v_readfirstlane_b32 s36, v139
	s_waitcnt lgkmcnt(1)
	v_readfirstlane_b32 s46, v141
	v_readfirstlane_b32 s50, v142
	v_readfirstlane_b32 s54, v143
	s_waitcnt lgkmcnt(0)
	v_readfirstlane_b32 s68, v145
	v_readfirstlane_b32 s72, v146
	v_readfirstlane_b32 s80, v147
	s_lshl_b64 s[10:11], s[10:11], 10
	v_readfirstlane_b32 s4, v136
	s_cmp_ge_i32 vcc_hi, 4
	s_cselect_b64 s[100:101], s[6:7], 0
	s_not_b64 exec, s[100:101]
	s_waitcnt vmcnt(47)
	global_store_dwordx4 v[148:149], v[26:29], off nt
	s_waitcnt vmcnt(47)
	global_store_dwordx4 v[150:151], v[18:21], off nt
	s_waitcnt vmcnt(47)
	global_store_dwordx4 v[152:153], v[10:13], off nt
	s_waitcnt vmcnt(47)
	global_store_dwordx4 v[154:155], v[2:5], off nt
	s_waitcnt vmcnt(38)
	global_store_dwordx4 v[156:157], v[30:33], off nt
	s_waitcnt vmcnt(47)
	global_store_dwordx4 v[158:159], v[14:17], off nt
	s_waitcnt vmcnt(47)
	global_store_dwordx4 v[160:161], v[6:9], off nt
	s_waitcnt vmcnt(47)
	global_store_dwordx4 v[166:167], v[22:25], off nt
	s_waitcnt vmcnt(41)
	global_store_dwordx4 v[168:169], v[58:61], off nt
	s_waitcnt vmcnt(47)
	global_store_dwordx4 v[170:171], v[54:57], off nt
	s_waitcnt vmcnt(47)
	global_store_dwordx4 v[172:173], v[46:49], off nt
	s_waitcnt vmcnt(47)
	global_store_dwordx4 v[174:175], v[34:37], off nt
	s_waitcnt vmcnt(44)
	global_store_dwordx4 v[176:177], v[62:65], off nt
	s_waitcnt vmcnt(47)
	global_store_dwordx4 v[178:179], v[50:53], off nt
	s_waitcnt vmcnt(47)
	global_store_dwordx4 v[180:181], v[42:45], off nt
	s_waitcnt vmcnt(47)
	global_store_dwordx4 v[182:183], v[38:41], off nt
	s_mov_b64 exec, -1
	s_lshl_b64 s[22:23], s[22:23], 10
	s_lshl_b64 s[24:25], s[24:25], 10
	s_lshl_b64 s[28:29], s[28:29], 10
	s_lshl_b64 s[34:35], s[34:35], 10
	s_lshl_b64 s[36:37], s[36:37], 10
	s_lshl_b64 s[46:47], s[46:47], 10
	s_lshl_b64 s[50:51], s[50:51], 10
	s_lshl_b64 s[54:55], s[54:55], 10
	s_lshl_b64 s[68:69], s[68:69], 10
	s_lshl_b64 s[72:73], s[72:73], 10
	s_lshl_b64 s[80:81], s[80:81], 10
	v_lshl_add_u64 v[2:3], v[130:131], 0, s[10:11]
	s_lshl_b64 s[10:11], s[4:5], 10
	v_readfirstlane_b32 s4, v140
	v_lshl_add_u64 v[4:5], v[130:131], 0, s[22:23]
	v_lshl_add_u64 v[6:7], v[130:131], 0, s[24:25]
	v_lshl_add_u64 v[8:9], v[130:131], 0, s[28:29]
	v_lshl_add_u64 v[22:23], v[130:131], 0, s[34:35]
	v_lshl_add_u64 v[24:25], v[130:131], 0, s[36:37]
	v_lshl_add_u64 v[30:31], v[130:131], 0, s[46:47]
	v_lshl_add_u64 v[32:33], v[130:131], 0, s[50:51]
	v_lshl_add_u64 v[34:35], v[130:131], 0, s[54:55]
	v_lshl_add_u64 v[38:39], v[130:131], 0, s[68:69]
	v_lshl_add_u64 v[40:41], v[130:131], 0, s[72:73]
	v_lshl_add_u64 v[58:59], v[130:131], 0, s[80:81]
	v_lshl_add_u64 v[60:61], v[130:131], 0, s[10:11]
	s_lshl_b64 s[10:11], s[4:5], 10
	v_readfirstlane_b32 s4, v144
	global_load_dwordx4 v[26:29], v[184:185], off
	global_load_dwordx4 v[18:21], v[2:3], off
	global_load_dwordx4 v[10:13], v[4:5], off
	s_nop 0
	global_load_dwordx4 v[2:5], v[6:7], off
	global_load_dwordx4 v[14:17], v[8:9], off
	s_nop 0
	global_load_dwordx4 v[6:9], v[22:23], off
	s_nop 0
	global_load_dwordx4 v[22:25], v[24:25], off
	s_nop 0
	global_load_dwordx4 v[54:57], v[30:31], off
	global_load_dwordx4 v[46:49], v[32:33], off
	s_nop 0
	global_load_dwordx4 v[34:37], v[34:35], off
	s_nop 0
	global_load_dwordx4 v[50:53], v[38:39], off
	global_load_dwordx4 v[42:45], v[40:41], off
	s_nop 0
	global_load_dwordx4 v[38:41], v[58:59], off
	global_load_dwordx4 v[30:33], v[60:61], off
	v_lshl_add_u64 v[58:59], v[130:131], 0, s[10:11]
	s_lshl_b64 s[10:11], s[4:5], 10
	s_mov_b64 s[8:9], s[18:19]
	s_mov_b64 s[12:13], s[14:15]
	v_lshl_add_u64 v[62:63], v[130:131], 0, s[10:11]
	global_load_dwordx4 v[58:61], v[58:59], off
	s_add_i32 s4, s26, s98
	global_load_dwordx4 v[62:65], v[62:63], off
	s_waitcnt vmcnt(63) expcnt(7) lgkmcnt(15)
	s_barrier
	ds_read_b128 v[130:133], v165 offset:64
	ds_read_b128 v[134:137], v165 offset:80
	ds_read_b128 v[138:141], v165 offset:96
	ds_read_b128 v[142:145], v165 offset:112
	s_lshl_b64 s[10:11], s[4:5], 10
	s_or_b32 s40, s4, 1
	s_or_b32 s48, s4, 2
	s_or_b32 s52, s4, 3
	s_or_b32 s58, s4, 4
	s_or_b32 s64, s4, 5
	s_or_b32 s66, s4, 6
	s_or_b32 s74, s4, 7
	s_or_b32 s82, s4, 8
	s_or_b32 s84, s4, 9
	s_or_b32 s86, s4, 10
	s_or_b32 s90, s4, 11
	s_or_b32 s92, s4, 12
	s_or_b32 s96, s4, 13
	s_or_b32 s94, s4, 14
	s_or_b32 s4, s4, 15
	s_mov_b32 s41, s5
	s_mov_b32 s49, s5
	s_mov_b32 s53, s5
	s_mov_b32 s59, s5
	s_mov_b32 s65, s5
	s_mov_b32 s67, s5
	s_mov_b32 s75, s5
	s_mov_b32 s83, s5
	s_mov_b32 s85, s5
	s_mov_b32 s87, s5
	s_mov_b32 s91, s5
	s_mov_b32 s93, s5
	s_mov_b32 s97, s5
	s_mov_b32 s95, s5
	s_lshl_b64 s[68:69], s[4:5], 10
	v_lshl_add_u64 v[146:147], s[12:13], 0, v[162:163]
	s_waitcnt lgkmcnt(3)
	v_readfirstlane_b32 s4, v130
	s_mov_b32 s89, s5
	s_mov_b32 s79, s5
	s_mov_b32 s77, s5
	s_mov_b32 s71, s5
	s_mov_b32 s63, s5
	s_mov_b32 s61, s5
	s_mov_b32 s57, s5
	s_mov_b32 s45, s5
	s_mov_b32 s43, s5
	s_mov_b32 s39, s5
	s_mov_b32 s31, s5
	s_mov_b32 s27, s5
	s_lshl_b64 s[22:23], s[40:41], 10
	s_lshl_b64 s[24:25], s[48:49], 10
	s_lshl_b64 s[28:29], s[52:53], 10
	s_lshl_b64 s[34:35], s[58:59], 10
	s_lshl_b64 s[36:37], s[64:65], 10
	s_lshl_b64 s[40:41], s[66:67], 10
	s_lshl_b64 s[46:47], s[74:75], 10
	s_lshl_b64 s[48:49], s[82:83], 10
	s_lshl_b64 s[50:51], s[84:85], 10
	s_lshl_b64 s[52:53], s[86:87], 10
	s_lshl_b64 s[54:55], s[90:91], 10
	s_lshl_b64 s[58:59], s[92:93], 10
	s_lshl_b64 s[64:65], s[96:97], 10
	s_lshl_b64 s[66:67], s[94:95], 10
	v_lshl_add_u64 v[148:149], s[8:9], 0, v[162:163]
	v_lshl_add_u64 v[150:151], v[146:147], 0, s[10:11]
	v_readfirstlane_b32 s88, v131
	v_readfirstlane_b32 s78, v132
	v_readfirstlane_b32 s76, v133
	s_waitcnt lgkmcnt(2)
	v_readfirstlane_b32 s70, v135
	v_readfirstlane_b32 s62, v136
	v_readfirstlane_b32 s60, v137
	s_waitcnt lgkmcnt(1)
	v_readfirstlane_b32 s56, v139
	v_readfirstlane_b32 s44, v140
	v_readfirstlane_b32 s42, v141
	s_waitcnt lgkmcnt(0)
	v_readfirstlane_b32 s38, v143
	v_readfirstlane_b32 s30, v144
	v_readfirstlane_b32 s26, v145
	s_lshl_b64 s[8:9], s[4:5], 10
	v_readfirstlane_b32 s4, v134
	v_lshl_add_u64 v[152:153], v[146:147], 0, s[22:23]
	v_lshl_add_u64 v[154:155], v[146:147], 0, s[24:25]
	v_lshl_add_u64 v[156:157], v[146:147], 0, s[28:29]
	v_lshl_add_u64 v[158:159], v[146:147], 0, s[34:35]
	v_lshl_add_u64 v[160:161], v[146:147], 0, s[36:37]
	v_lshl_add_u64 v[166:167], v[146:147], 0, s[40:41]
	v_lshl_add_u64 v[168:169], v[146:147], 0, s[46:47]
	v_lshl_add_u64 v[170:171], v[146:147], 0, s[48:49]
	v_lshl_add_u64 v[172:173], v[146:147], 0, s[50:51]
	v_lshl_add_u64 v[174:175], v[146:147], 0, s[52:53]
	v_lshl_add_u64 v[176:177], v[146:147], 0, s[54:55]
	v_lshl_add_u64 v[178:179], v[146:147], 0, s[58:59]
	v_lshl_add_u64 v[180:181], v[146:147], 0, s[64:65]
	v_lshl_add_u64 v[182:183], v[146:147], 0, s[66:67]
	v_lshl_add_u64 v[146:147], v[146:147], 0, s[68:69]
	s_cmp_ge_i32 vcc_hi, 4
	s_cselect_b64 s[100:101], s[6:7], 0
	s_not_b64 exec, s[100:101]
	s_waitcnt vmcnt(47)
	global_store_dwordx4 v[150:151], v[78:81], off nt
	s_waitcnt vmcnt(47)
	global_store_dwordx4 v[152:153], v[74:77], off nt
	s_waitcnt vmcnt(47)
	global_store_dwordx4 v[154:155], v[70:73], off nt
	s_waitcnt vmcnt(47)
	global_store_dwordx4 v[156:157], v[66:69], off nt
	s_waitcnt vmcnt(38)
	global_store_dwordx4 v[158:159], v[118:121], off nt
	global_store_dwordx4 v[160:161], v[86:89], off nt
	global_store_dwordx4 v[166:167], v[82:85], off nt
	global_store_dwordx4 v[168:169], v[90:93], off nt
	s_waitcnt vmcnt(41)
	global_store_dwordx4 v[170:171], v[126:129], off nt
	global_store_dwordx4 v[172:173], v[102:105], off nt
	global_store_dwordx4 v[174:175], v[98:101], off nt
	global_store_dwordx4 v[176:177], v[94:97], off nt
	s_waitcnt vmcnt(44)
	global_store_dwordx4 v[178:179], v[122:125], off nt
	global_store_dwordx4 v[180:181], v[110:113], off nt
	global_store_dwordx4 v[182:183], v[106:109], off nt
	global_store_dwordx4 v[146:147], v[114:117], off nt
	s_mov_b64 exec, -1
	s_lshl_b64 s[10:11], s[88:89], 10
	s_lshl_b64 s[12:13], s[78:79], 10
	s_lshl_b64 s[22:23], s[76:77], 10
	s_lshl_b64 s[24:25], s[70:71], 10
	s_lshl_b64 s[28:29], s[62:63], 10
	s_lshl_b64 s[34:35], s[60:61], 10
	s_lshl_b64 s[36:37], s[56:57], 10
	s_lshl_b64 s[40:41], s[44:45], 10
	s_lshl_b64 s[42:43], s[42:43], 10
	s_lshl_b64 s[38:39], s[38:39], 10
	s_lshl_b64 s[30:31], s[30:31], 10
	s_lshl_b64 s[26:27], s[26:27], 10
	v_lshl_add_u64 v[66:67], v[148:149], 0, s[8:9]
	s_lshl_b64 s[8:9], s[4:5], 10
	v_lshl_add_u64 v[82:83], v[148:149], 0, s[10:11]
	v_lshl_add_u64 v[84:85], v[148:149], 0, s[12:13]
	v_lshl_add_u64 v[86:87], v[148:149], 0, s[22:23]
	v_lshl_add_u64 v[94:95], v[148:149], 0, s[24:25]
	v_lshl_add_u64 v[96:97], v[148:149], 0, s[28:29]
	v_lshl_add_u64 v[98:99], v[148:149], 0, s[34:35]
	v_lshl_add_u64 v[106:107], v[148:149], 0, s[36:37]
	v_lshl_add_u64 v[108:109], v[148:149], 0, s[40:41]
	v_lshl_add_u64 v[110:111], v[148:149], 0, s[42:43]
	v_lshl_add_u64 v[114:115], v[148:149], 0, s[38:39]
	v_lshl_add_u64 v[116:117], v[148:149], 0, s[30:31]
	v_lshl_add_u64 v[118:119], v[148:149], 0, s[26:27]
	v_lshl_add_u64 v[120:121], v[148:149], 0, s[8:9]
	v_readfirstlane_b32 s4, v138
	global_load_dwordx4 v[78:81], v[66:67], off
	global_load_dwordx4 v[74:77], v[82:83], off
	global_load_dwordx4 v[70:73], v[84:85], off
	s_nop 0
	global_load_dwordx4 v[66:69], v[86:87], off
	s_nop 0
	global_load_dwordx4 v[86:89], v[94:95], off
	global_load_dwordx4 v[82:85], v[96:97], off
	global_load_dwordx4 v[90:93], v[98:99], off
	global_load_dwordx4 v[102:105], v[106:107], off
	s_nop 0
	global_load_dwordx4 v[98:101], v[108:109], off
	global_load_dwordx4 v[94:97], v[110:111], off
	s_nop 0
	global_load_dwordx4 v[110:113], v[114:115], off
	global_load_dwordx4 v[106:109], v[116:117], off
	s_nop 0
	global_load_dwordx4 v[114:117], v[118:119], off
	s_nop 0
	global_load_dwordx4 v[118:121], v[120:121], off
	s_lshl_b64 s[8:9], s[4:5], 10
	v_readfirstlane_b32 s4, v142
	v_lshl_add_u64 v[122:123], v[148:149], 0, s[8:9]
	s_lshl_b64 s[8:9], s[4:5], 10
	global_load_dwordx4 v[126:129], v[122:123], off
	v_lshl_add_u64 v[122:123], v[148:149], 0, s[8:9]
	global_load_dwordx4 v[122:125], v[122:123], off
	s_add_i32 vcc_hi, vcc_hi, 2
	s_add_i32 s99, s99, 32
	s_addk_i32 vcc_lo, 0x2000
	s_addk_i32 s3, 0x80
	s_cmp_gt_u32 vcc_hi, 5
	s_waitcnt vmcnt(63) expcnt(7) lgkmcnt(15)
	s_barrier
	s_cbranch_scc0 .LBB1_107
	s_barrier
	ds_read_b32 v130, v1
	s_waitcnt lgkmcnt(0)
	v_cmp_gt_i32_e32 vcc, 1, v130
	s_cbranch_vccnz .LBB1_111

.LBB1_151:
	s_barrier
	s_add_i32 s100, s98, 0xfffe7f90
	s_add_i32 s6, s33, -5
	s_lshl_b32 s6, s6, 3
	s_add_i32 s100, s100, s6
	s_lshl_b32 s7, s6, 2
	s_add_i32 s7, s7, 0x22640
	v_mov_b32_e32 v114, s7
	ds_read_b128 v[2:5], v114 offset:0
	ds_read_b128 v[6:9], v114 offset:16
	s_waitcnt lgkmcnt(0)
	v_lshl_or_b32 v106, v2, 10, v162
	v_lshl_or_b32 v107, v3, 10, v162
	v_lshl_or_b32 v108, v4, 10, v162
	v_lshl_or_b32 v109, v5, 10, v162
	v_lshl_or_b32 v110, v6, 10, v162
	v_lshl_or_b32 v111, v7, 10, v162
	v_lshl_or_b32 v112, v8, 10, v162
	v_lshl_or_b32 v113, v9, 10, v162
	global_load_dwordx4 v[10:13], v106, s[18:19]
	global_load_dwordx4 v[14:17], v107, s[18:19]
	global_load_dwordx4 v[18:21], v108, s[18:19]
	global_load_dwordx4 v[22:25], v109, s[18:19]
	global_load_dwordx4 v[26:29], v110, s[18:19]
	global_load_dwordx4 v[30:33], v111, s[18:19]
	global_load_dwordx4 v[34:37], v112, s[18:19]
	global_load_dwordx4 v[38:41], v113, s[18:19]
	ds_read_b128 v[2:5], v114 offset:64
	ds_read_b128 v[6:9], v114 offset:80
	s_waitcnt lgkmcnt(0)
	v_lshl_or_b32 v106, v2, 10, v162
	v_lshl_or_b32 v107, v3, 10, v162
	v_lshl_or_b32 v108, v4, 10, v162
	v_lshl_or_b32 v109, v5, 10, v162
	v_lshl_or_b32 v110, v6, 10, v162
	v_lshl_or_b32 v111, v7, 10, v162
	v_lshl_or_b32 v112, v8, 10, v162
	v_lshl_or_b32 v113, v9, 10, v162
	global_load_dwordx4 v[42:45], v106, s[18:19]
	global_load_dwordx4 v[46:49], v107, s[18:19]
	global_load_dwordx4 v[50:53], v108, s[18:19]
	global_load_dwordx4 v[54:57], v109, s[18:19]
	global_load_dwordx4 v[58:61], v110, s[18:19]
	global_load_dwordx4 v[62:65], v111, s[18:19]
	global_load_dwordx4 v[66:69], v112, s[18:19]
	global_load_dwordx4 v[70:73], v113, s[18:19]
	ds_read_b128 v[2:5], v114 offset:128
	ds_read_b128 v[6:9], v114 offset:144
	s_waitcnt lgkmcnt(0)
	v_lshl_or_b32 v106, v2, 10, v162
	v_lshl_or_b32 v107, v3, 10, v162
	v_lshl_or_b32 v108, v4, 10, v162
	v_lshl_or_b32 v109, v5, 10, v162
	v_lshl_or_b32 v110, v6, 10, v162
	v_lshl_or_b32 v111, v7, 10, v162
	v_lshl_or_b32 v112, v8, 10, v162
	v_lshl_or_b32 v113, v9, 10, v162
	global_load_dwordx4 v[74:77], v106, s[18:19]
	global_load_dwordx4 v[78:81], v107, s[18:19]
	global_load_dwordx4 v[82:85], v108, s[18:19]
	global_load_dwordx4 v[86:89], v109, s[18:19]
	global_load_dwordx4 v[90:93], v110, s[18:19]
	global_load_dwordx4 v[94:97], v111, s[18:19]
	global_load_dwordx4 v[98:101], v112, s[18:19]
	global_load_dwordx4 v[102:105], v113, s[18:19]
	s_add_i32 s2, s100, 0
	s_lshl_b32 s2, s2, 10
	s_add_u32 s2, s14, s2
	s_addc_u32 s3, s15, 0
	s_add_u32 s4, s2, 0x1000
	s_addc_u32 s5, s3, 0
	s_waitcnt vmcnt(16)
	global_store_dwordx4 v162, v[10:13], s[2:3] offset:0 nt
	global_store_dwordx4 v162, v[14:17], s[2:3] offset:1024 nt
	global_store_dwordx4 v162, v[18:21], s[2:3] offset:2048 nt
	global_store_dwordx4 v162, v[22:25], s[2:3] offset:3072 nt
	global_store_dwordx4 v162, v[26:29], s[4:5] offset:0 nt
	global_store_dwordx4 v162, v[30:33], s[4:5] offset:1024 nt
	global_store_dwordx4 v162, v[34:37], s[4:5] offset:2048 nt
	global_store_dwordx4 v162, v[38:41], s[4:5] offset:3072 nt
	s_barrier
	ds_read_b128 v[2:5], v114 offset:192
	ds_read_b128 v[6:9], v114 offset:208
	s_waitcnt lgkmcnt(0)
	v_lshl_or_b32 v106, v2, 10, v162
	v_lshl_or_b32 v107, v3, 10, v162
	v_lshl_or_b32 v108, v4, 10, v162
	v_lshl_or_b32 v109, v5, 10, v162
	v_lshl_or_b32 v110, v6, 10, v162
	v_lshl_or_b32 v111, v7, 10, v162
	v_lshl_or_b32 v112, v8, 10, v162
	v_lshl_or_b32 v113, v9, 10, v162
	global_load_dwordx4 v[10:13], v106, s[18:19]
	global_load_dwordx4 v[14:17], v107, s[18:19]
	global_load_dwordx4 v[18:21], v108, s[18:19]
	global_load_dwordx4 v[22:25], v109, s[18:19]
	global_load_dwordx4 v[26:29], v110, s[18:19]
	global_load_dwordx4 v[30:33], v111, s[18:19]
	global_load_dwordx4 v[34:37], v112, s[18:19]
	global_load_dwordx4 v[38:41], v113, s[18:19]
	s_add_i32 s2, s100, 16
	s_lshl_b32 s2, s2, 10
	s_add_u32 s2, s14, s2
	s_addc_u32 s3, s15, 0
	s_add_u32 s4, s2, 0x1000
	s_addc_u32 s5, s3, 0
	s_waitcnt vmcnt(24)
	global_store_dwordx4 v162, v[42:45], s[2:3] offset:0 nt
	global_store_dwordx4 v162, v[46:49], s[2:3] offset:1024 nt
	global_store_dwordx4 v162, v[50:53], s[2:3] offset:2048 nt
	global_store_dwordx4 v162, v[54:57], s[2:3] offset:3072 nt
	global_store_dwordx4 v162, v[58:61], s[4:5] offset:0 nt
	global_store_dwordx4 v162, v[62:65], s[4:5] offset:1024 nt
	global_store_dwordx4 v162, v[66:69], s[4:5] offset:2048 nt
	global_store_dwordx4 v162, v[70:73], s[4:5] offset:3072 nt
	s_barrier
	ds_read_b128 v[2:5], v114 offset:256
	ds_read_b128 v[6:9], v114 offset:272
	s_waitcnt lgkmcnt(0)
	v_lshl_or_b32 v106, v2, 10, v162
	v_lshl_or_b32 v107, v3, 10, v162
	v_lshl_or_b32 v108, v4, 10, v162
	v_lshl_or_b32 v109, v5, 10, v162
	v_lshl_or_b32 v110, v6, 10, v162
	v_lshl_or_b32 v111, v7, 10, v162
	v_lshl_or_b32 v112, v8, 10, v162
	v_lshl_or_b32 v113, v9, 10, v162
	global_load_dwordx4 v[42:45], v106, s[18:19]
	global_load_dwordx4 v[46:49], v107, s[18:19]
	global_load_dwordx4 v[50:53], v108, s[18:19]
	global_load_dwordx4 v[54:57], v109, s[18:19]
	global_load_dwordx4 v[58:61], v110, s[18:19]
	global_load_dwordx4 v[62:65], v111, s[18:19]
	global_load_dwordx4 v[66:69], v112, s[18:19]
	global_load_dwordx4 v[70:73], v113, s[18:19]
	s_add_i32 s2, s100, 32
	s_lshl_b32 s2, s2, 10
	s_add_u32 s2, s14, s2
	s_addc_u32 s3, s15, 0
	s_add_u32 s4, s2, 0x1000
	s_addc_u32 s5, s3, 0
	s_waitcnt vmcnt(32)
	global_store_dwordx4 v162, v[74:77], s[2:3] offset:0 nt
	global_store_dwordx4 v162, v[78:81], s[2:3] offset:1024 nt
	global_store_dwordx4 v162, v[82:85], s[2:3] offset:2048 nt
	global_store_dwordx4 v162, v[86:89], s[2:3] offset:3072 nt
	global_store_dwordx4 v162, v[90:93], s[4:5] offset:0 nt
	global_store_dwordx4 v162, v[94:97], s[4:5] offset:1024 nt
	global_store_dwordx4 v162, v[98:101], s[4:5] offset:2048 nt
	global_store_dwordx4 v162, v[102:105], s[4:5] offset:3072 nt
	s_barrier
	ds_read_b128 v[2:5], v114 offset:320
	ds_read_b128 v[6:9], v114 offset:336
	s_waitcnt lgkmcnt(0)
	v_lshl_or_b32 v106, v2, 10, v162
	v_lshl_or_b32 v107, v3, 10, v162
	v_lshl_or_b32 v108, v4, 10, v162
	v_lshl_or_b32 v109, v5, 10, v162
	v_lshl_or_b32 v110, v6, 10, v162
	v_lshl_or_b32 v111, v7, 10, v162
	v_lshl_or_b32 v112, v8, 10, v162
	v_lshl_or_b32 v113, v9, 10, v162
	global_load_dwordx4 v[74:77], v106, s[18:19]
	global_load_dwordx4 v[78:81], v107, s[18:19]
	global_load_dwordx4 v[82:85], v108, s[18:19]
	global_load_dwordx4 v[86:89], v109, s[18:19]
	global_load_dwordx4 v[90:93], v110, s[18:19]
	global_load_dwordx4 v[94:97], v111, s[18:19]
	global_load_dwordx4 v[98:101], v112, s[18:19]
	global_load_dwordx4 v[102:105], v113, s[18:19]
	s_add_i32 s2, s100, 48
	s_lshl_b32 s2, s2, 10
	s_add_u32 s2, s14, s2
	s_addc_u32 s3, s15, 0
	s_add_u32 s4, s2, 0x1000
	s_addc_u32 s5, s3, 0
	s_waitcnt vmcnt(32)
	global_store_dwordx4 v162, v[10:13], s[2:3] offset:0 nt
	global_store_dwordx4 v162, v[14:17], s[2:3] offset:1024 nt
	global_store_dwordx4 v162, v[18:21], s[2:3] offset:2048 nt
	global_store_dwordx4 v162, v[22:25], s[2:3] offset:3072 nt
	global_store_dwordx4 v162, v[26:29], s[4:5] offset:0 nt
	global_store_dwordx4 v162, v[30:33], s[4:5] offset:1024 nt
	global_store_dwordx4 v162, v[34:37], s[4:5] offset:2048 nt
	global_store_dwordx4 v162, v[38:41], s[4:5] offset:3072 nt
	s_barrier
	ds_read_b128 v[2:5], v114 offset:768
	ds_read_b128 v[6:9], v114 offset:784
	s_waitcnt lgkmcnt(0)
	v_lshl_or_b32 v106, v2, 10, v162
	v_lshl_or_b32 v107, v3, 10, v162
	v_lshl_or_b32 v108, v4, 10, v162
	v_lshl_or_b32 v109, v5, 10, v162
	v_lshl_or_b32 v110, v6, 10, v162
	v_lshl_or_b32 v111, v7, 10, v162
	v_lshl_or_b32 v112, v8, 10, v162
	v_lshl_or_b32 v113, v9, 10, v162
	global_load_dwordx4 v[10:13], v106, s[18:19]
	global_load_dwordx4 v[14:17], v107, s[18:19]
	global_load_dwordx4 v[18:21], v108, s[18:19]
	global_load_dwordx4 v[22:25], v109, s[18:19]
	global_load_dwordx4 v[26:29], v110, s[18:19]
	global_load_dwordx4 v[30:33], v111, s[18:19]
	global_load_dwordx4 v[34:37], v112, s[18:19]
	global_load_dwordx4 v[38:41], v113, s[18:19]
	s_add_i32 s2, s100, 64
	s_lshl_b32 s2, s2, 10
	s_add_u32 s2, s14, s2
	s_addc_u32 s3, s15, 0
	s_add_u32 s4, s2, 0x1000
	s_addc_u32 s5, s3, 0
	s_waitcnt vmcnt(32)
	global_store_dwordx4 v162, v[42:45], s[2:3] offset:0 nt
	global_store_dwordx4 v162, v[46:49], s[2:3] offset:1024 nt
	global_store_dwordx4 v162, v[50:53], s[2:3] offset:2048 nt
	global_store_dwordx4 v162, v[54:57], s[2:3] offset:3072 nt
	global_store_dwordx4 v162, v[58:61], s[4:5] offset:0 nt
	global_store_dwordx4 v162, v[62:65], s[4:5] offset:1024 nt
	global_store_dwordx4 v162, v[66:69], s[4:5] offset:2048 nt
	global_store_dwordx4 v162, v[70:73], s[4:5] offset:3072 nt
	s_barrier
	ds_read_b128 v[2:5], v114 offset:832
	ds_read_b128 v[6:9], v114 offset:848
	s_waitcnt lgkmcnt(0)
	v_lshl_or_b32 v106, v2, 10, v162
	v_lshl_or_b32 v107, v3, 10, v162
	v_lshl_or_b32 v108, v4, 10, v162
	v_lshl_or_b32 v109, v5, 10, v162
	v_lshl_or_b32 v110, v6, 10, v162
	v_lshl_or_b32 v111, v7, 10, v162
	v_lshl_or_b32 v112, v8, 10, v162
	v_lshl_or_b32 v113, v9, 10, v162
	global_load_dwordx4 v[42:45], v106, s[18:19]
	global_load_dwordx4 v[46:49], v107, s[18:19]
	global_load_dwordx4 v[50:53], v108, s[18:19]
	global_load_dwordx4 v[54:57], v109, s[18:19]
	global_load_dwordx4 v[58:61], v110, s[18:19]
	global_load_dwordx4 v[62:65], v111, s[18:19]
	global_load_dwordx4 v[66:69], v112, s[18:19]
	global_load_dwordx4 v[70:73], v113, s[18:19]
	s_add_i32 s2, s100, 80
	s_lshl_b32 s2, s2, 10
	s_add_u32 s2, s14, s2
	s_addc_u32 s3, s15, 0
	s_add_u32 s4, s2, 0x1000
	s_addc_u32 s5, s3, 0
	s_waitcnt vmcnt(32)
	global_store_dwordx4 v162, v[74:77], s[2:3] offset:0 nt
	global_store_dwordx4 v162, v[78:81], s[2:3] offset:1024 nt
	global_store_dwordx4 v162, v[82:85], s[2:3] offset:2048 nt
	global_store_dwordx4 v162, v[86:89], s[2:3] offset:3072 nt
	global_store_dwordx4 v162, v[90:93], s[4:5] offset:0 nt
	global_store_dwordx4 v162, v[94:97], s[4:5] offset:1024 nt
	global_store_dwordx4 v162, v[98:101], s[4:5] offset:2048 nt
	global_store_dwordx4 v162, v[102:105], s[4:5] offset:3072 nt
	s_barrier
	s_add_i32 s2, s100, 32832
	s_lshl_b32 s2, s2, 10
	s_add_u32 s2, s14, s2
	s_addc_u32 s3, s15, 0
	s_add_u32 s4, s2, 0x1000
	s_addc_u32 s5, s3, 0
	s_waitcnt vmcnt(24)
	global_store_dwordx4 v162, v[10:13], s[2:3] offset:0 nt
	global_store_dwordx4 v162, v[14:17], s[2:3] offset:1024 nt
	global_store_dwordx4 v162, v[18:21], s[2:3] offset:2048 nt
	global_store_dwordx4 v162, v[22:25], s[2:3] offset:3072 nt
	global_store_dwordx4 v162, v[26:29], s[4:5] offset:0 nt
	global_store_dwordx4 v162, v[30:33], s[4:5] offset:1024 nt
	global_store_dwordx4 v162, v[34:37], s[4:5] offset:2048 nt
	global_store_dwordx4 v162, v[38:41], s[4:5] offset:3072 nt
	s_barrier
	s_add_i32 s2, s100, 32848
	s_lshl_b32 s2, s2, 10
	s_add_u32 s2, s14, s2
	s_addc_u32 s3, s15, 0
	s_add_u32 s4, s2, 0x1000
	s_addc_u32 s5, s3, 0
	s_waitcnt vmcnt(16)
	global_store_dwordx4 v162, v[42:45], s[2:3] offset:0 nt
	global_store_dwordx4 v162, v[46:49], s[2:3] offset:1024 nt
	global_store_dwordx4 v162, v[50:53], s[2:3] offset:2048 nt
	global_store_dwordx4 v162, v[54:57], s[2:3] offset:3072 nt
	global_store_dwordx4 v162, v[58:61], s[4:5] offset:0 nt
	global_store_dwordx4 v162, v[62:65], s[4:5] offset:1024 nt
	global_store_dwordx4 v162, v[66:69], s[4:5] offset:2048 nt
	global_store_dwordx4 v162, v[70:73], s[4:5] offset:3072 nt
	s_barrier
	s_barrier
	ds_read_b32 v1, v1
	s_waitcnt lgkmcnt(0)
	v_cmp_gt_i32_e32 vcc, 1, v1
	s_cbranch_vccnz .LBB1_154
